# s12 + OUT epilogue tile stores (x1/out f32, hn f16) write-through (sc1)
# baseline (speedup 1.0000x reference)
; __device__ __forceinline__ unsigned cvt_pk_f16(float lo, float hi) { f32x2 v = {lo, hi}; h16x2 b = __builtin_convertvector(v, h16x2); return __builtin_bit_cast(unsigned, b); }
;     __device__ __forceinline__ void fused(f32x4 (&acc)[2][2][4][2], const Unit& u, int wr, int wc, int fr, int fq, PG8_LAS unsigned char* lds, int wid, int lane) const {
;     ...
;             for (int m = 0; m < 4; ++m) { const int r = ai * HALF + wr * 64 + m * 16 + fr2; const float rstd = bad ? qnan : S[r]; const size_t off = (size_t)(u.pm * BM + r) * DM + col2;
; #pragma unroll
;                 for (int bj = 0; bj < 2; ++bj)
; #pragma unroll
;                     for (int n = 0; n < 2; ++n) { const f32x4 x1 = acc[ai][bj][m][n]; const f32x4 y = x1 * rstd * gv[bj][n];
;                         if (FINAL) *(f32x4*)(out + off + bj * HALF + n * 16) = y;
;                         else { *(f32x4*)(out + off + bj * HALF + n * 16) = x1;
;                             typedef unsigned u32x2 __attribute__((ext_vector_type(2)));
;                             u32x2 w; w.x = cvt_pk_f16(y[0], y[1]); w.y = cvt_pk_f16(y[2], y[3]); *(u32x2*)(hn + off + bj * HALF + n * 16) = w; } } }
.LBB0_194:
	v_add_u32_e32 v116, s28, v121
	v_ashrrev_i32_e32 v117, 31, v116
	v_lshlrev_b64 v[134:135], 12, v[116:117]
	s_waitcnt lgkmcnt(0)
	v_pk_mul_f32 v[130:131], v[238:239], v[120:121] op_sel_hi:[1,0]
	v_pk_mul_f32 v[136:137], v[240:241], v[120:121] op_sel_hi:[1,0]
	v_lshl_add_u64 v[134:135], s[14:15], 0, v[134:135]
	s_waitcnt vmcnt(3)
	v_pk_mul_f32 v[132:133], v[14:15], v[130:131]
	v_pk_mul_f32 v[130:131], v[12:13], v[136:137]
	v_lshl_add_u64 v[134:135], v[114:115], 2, v[134:135]
	global_store_dwordx4 v[134:135], v[130:133], off sc1
	v_pk_mul_f32 v[136:137], v[236:237], v[120:121] op_sel_hi:[1,0]
	v_cndmask_b32_e64 v117, 0, 1, s[0:1]
	v_pk_mul_f32 v[130:131], v[234:235], v[120:121] op_sel_hi:[1,0]
	v_cmp_ne_u32_e64 s[38:39], 1, v117
	s_waitcnt vmcnt(3)
	v_pk_mul_f32 v[132:133], v[10:11], v[130:131]
	v_pk_mul_f32 v[130:131], v[8:9], v[136:137]
	global_store_dwordx4 v[134:135], v[130:133], off offset:64 sc1
	v_pk_mul_f32 v[136:137], v[232:233], v[120:121] op_sel_hi:[1,0]
	s_andn2_b64 vcc, exec, s[0:1]
	v_pk_mul_f32 v[130:131], v[230:231], v[120:121] op_sel_hi:[1,0]
	s_waitcnt vmcnt(3)
	v_pk_mul_f32 v[132:133], v[6:7], v[130:131]
	v_pk_mul_f32 v[130:131], v[4:5], v[136:137]
	global_store_dwordx4 v[134:135], v[130:133], off offset:512 sc1
	v_pk_mul_f32 v[136:137], v[228:229], v[120:121] op_sel_hi:[1,0]
	s_nop 0
	v_pk_mul_f32 v[130:131], v[226:227], v[120:121] op_sel_hi:[1,0]
	s_waitcnt vmcnt(3)
	v_pk_mul_f32 v[132:133], v[2:3], v[130:131]
	v_pk_mul_f32 v[130:131], v[0:1], v[136:137]
	global_store_dwordx4 v[134:135], v[130:133], off offset:576 sc1
	s_cbranch_vccnz .LBB0_196
	v_lshl_add_u32 v96, v121, 2, 0
	ds_read_b32 v96, v96 offset:4160
.LBB0_196:
	s_nop 0
	v_add3_u32 v130, s28, v121, 16
	v_ashrrev_i32_e32 v131, 31, v130
	v_lshlrev_b64 v[130:131], 12, v[130:131]
	v_lshl_add_u64 v[130:131], s[14:15], 0, v[130:131]
	s_waitcnt lgkmcnt(0)
	v_pk_mul_f32 v[100:101], v[100:101], v[96:97] op_sel_hi:[1,0]
	v_pk_mul_f32 v[98:99], v[98:99], v[96:97] op_sel_hi:[1,0]
	v_pk_mul_f32 v[112:113], v[112:113], v[96:97] op_sel_hi:[1,0]
	v_pk_mul_f32 v[110:111], v[110:111], v[96:97] op_sel_hi:[1,0]
	v_lshl_add_u64 v[130:131], v[114:115], 2, v[130:131]
	v_pk_mul_f32 v[108:109], v[108:109], v[96:97] op_sel_hi:[1,0]
	v_pk_mul_f32 v[106:107], v[106:107], v[96:97] op_sel_hi:[1,0]
	v_pk_mul_f32 v[104:105], v[104:105], v[96:97] op_sel_hi:[1,0]
	v_pk_mul_f32 v[102:103], v[102:103], v[96:97] op_sel_hi:[1,0]
	v_pk_mul_f32 v[100:101], v[2:3], v[100:101]
	v_pk_mul_f32 v[98:99], v[0:1], v[98:99]
	v_pk_mul_f32 v[112:113], v[14:15], v[112:113]
	v_pk_mul_f32 v[110:111], v[12:13], v[110:111]
	v_pk_mul_f32 v[108:109], v[10:11], v[108:109]
	v_pk_mul_f32 v[106:107], v[8:9], v[106:107]
	v_pk_mul_f32 v[104:105], v[6:7], v[104:105]
	v_pk_mul_f32 v[102:103], v[4:5], v[102:103]
	global_store_dwordx4 v[130:131], v[98:101], off offset:576 sc1
	v_mov_b32_e32 v96, 0x7fc00000
	s_and_b64 vcc, exec, s[38:39]
	v_mov_b32_e32 v98, 0x7fc00000
	global_store_dwordx4 v[130:131], v[110:113], off sc1
	global_store_dwordx4 v[130:131], v[106:109], off offset:64 sc1
	global_store_dwordx4 v[130:131], v[102:105], off offset:512 sc1
	s_cbranch_vccnz .LBB0_198
	v_lshl_add_u32 v98, v121, 2, 0
	ds_read_b32 v98, v98 offset:4224
.LBB0_198:
	v_add3_u32 v100, s28, v121, 32
	v_ashrrev_i32_e32 v101, 31, v100
	v_lshlrev_b64 v[100:101], 12, v[100:101]
	s_waitcnt lgkmcnt(0)
	v_pk_mul_f32 v[94:95], v[94:95], v[98:99] op_sel_hi:[1,0]
	v_pk_mul_f32 v[92:93], v[92:93], v[98:99] op_sel_hi:[1,0]
	v_lshl_add_u64 v[100:101], s[14:15], 0, v[100:101]
	v_pk_mul_f32 v[90:91], v[90:91], v[98:99] op_sel_hi:[1,0]
	v_pk_mul_f32 v[88:89], v[88:89], v[98:99] op_sel_hi:[1,0]
	v_pk_mul_f32 v[86:87], v[86:87], v[98:99] op_sel_hi:[1,0]
	v_pk_mul_f32 v[84:85], v[84:85], v[98:99] op_sel_hi:[1,0]
	v_pk_mul_f32 v[82:83], v[82:83], v[98:99] op_sel_hi:[1,0]
	v_pk_mul_f32 v[80:81], v[80:81], v[98:99] op_sel_hi:[1,0]
	v_pk_mul_f32 v[94:95], v[14:15], v[94:95]
	v_pk_mul_f32 v[92:93], v[12:13], v[92:93]
	v_lshl_add_u64 v[100:101], v[114:115], 2, v[100:101]
	v_pk_mul_f32 v[90:91], v[10:11], v[90:91]
	v_pk_mul_f32 v[88:89], v[8:9], v[88:89]
	v_pk_mul_f32 v[86:87], v[6:7], v[86:87]
	v_pk_mul_f32 v[84:85], v[4:5], v[84:85]
	v_pk_mul_f32 v[82:83], v[2:3], v[82:83]
	v_pk_mul_f32 v[80:81], v[0:1], v[80:81]
	s_and_b64 vcc, exec, s[38:39]
	global_store_dwordx4 v[100:101], v[92:95], off sc1
	global_store_dwordx4 v[100:101], v[88:91], off offset:64 sc1
	global_store_dwordx4 v[100:101], v[84:87], off offset:512 sc1
	global_store_dwordx4 v[100:101], v[80:83], off offset:576 sc1
	s_cbranch_vccnz .LBB0_200
	s_nop 0
	v_lshl_add_u32 v80, v121, 2, 0
	ds_read_b32 v96, v80 offset:4288
.LBB0_200:
	s_nop 0
	v_add3_u32 v80, s28, v121, 48
	v_ashrrev_i32_e32 v81, 31, v80
	v_lshlrev_b64 v[80:81], 12, v[80:81]
	v_lshl_add_u64 v[80:81], s[14:15], 0, v[80:81]
	s_waitcnt lgkmcnt(0)
	v_pk_mul_f32 v[66:67], v[66:67], v[96:97] op_sel_hi:[1,0]
	v_pk_mul_f32 v[64:65], v[64:65], v[96:97] op_sel_hi:[1,0]
	v_pk_mul_f32 v[78:79], v[78:79], v[96:97] op_sel_hi:[1,0]
	v_pk_mul_f32 v[76:77], v[76:77], v[96:97] op_sel_hi:[1,0]
	v_lshl_add_u64 v[80:81], v[114:115], 2, v[80:81]
	v_pk_mul_f32 v[74:75], v[74:75], v[96:97] op_sel_hi:[1,0]
	v_pk_mul_f32 v[72:73], v[72:73], v[96:97] op_sel_hi:[1,0]
	v_pk_mul_f32 v[70:71], v[70:71], v[96:97] op_sel_hi:[1,0]
	v_pk_mul_f32 v[68:69], v[68:69], v[96:97] op_sel_hi:[1,0]
	v_pk_mul_f32 v[66:67], v[2:3], v[66:67]
	v_pk_mul_f32 v[64:65], v[0:1], v[64:65]
	v_pk_mul_f32 v[78:79], v[14:15], v[78:79]
	v_pk_mul_f32 v[76:77], v[12:13], v[76:77]
	v_pk_mul_f32 v[74:75], v[10:11], v[74:75]
	v_pk_mul_f32 v[72:73], v[8:9], v[72:73]
	v_pk_mul_f32 v[70:71], v[6:7], v[70:71]
	v_pk_mul_f32 v[68:69], v[4:5], v[68:69]
	global_store_dwordx4 v[80:81], v[64:67], off offset:576 sc1
	s_and_b64 vcc, exec, s[38:39]
	global_store_dwordx4 v[80:81], v[76:79], off sc1
	v_mov_b32_e32 v64, 0x7fc00000
	v_mov_b32_e32 v66, 0x7fc00000
	global_store_dwordx4 v[80:81], v[72:75], off offset:64 sc1
	global_store_dwordx4 v[80:81], v[68:71], off offset:512 sc1
	s_cbranch_vccnz .LBB0_202
	v_lshl_add_u32 v65, v121, 2, 0
	ds_read_b32 v66, v65 offset:4608
; __device__ __forceinline__ unsigned cvt_pk_f16(float lo, float hi) { f32x2 v = {lo, hi}; h16x2 b = __builtin_convertvector(v, h16x2); return __builtin_bit_cast(unsigned, b); }
;     __device__ __forceinline__ void fused(f32x4 (&acc)[2][2][4][2], const Unit& u, int wr, int wc, int fr, int fq, PG8_LAS unsigned char* lds, int wid, int lane) const {
;     ...
;             for (int m = 0; m < 4; ++m) { const int r = ai * HALF + wr * 64 + m * 16 + fr2; const float rstd = bad ? qnan : S[r]; const size_t off = (size_t)(u.pm * BM + r) * DM + col2;
; #pragma unroll
;                 for (int bj = 0; bj < 2; ++bj)
; #pragma unroll
;                     for (int n = 0; n < 2; ++n) { const f32x4 x1 = acc[ai][bj][m][n]; const f32x4 y = x1 * rstd * gv[bj][n];
;                         if (FINAL) *(f32x4*)(out + off + bj * HALF + n * 16) = y;
;                         else { *(f32x4*)(out + off + bj * HALF + n * 16) = x1;
;                             typedef unsigned u32x2 __attribute__((ext_vector_type(2)));
;                             u32x2 w; w.x = cvt_pk_f16(y[0], y[1]); w.y = cvt_pk_f16(y[2], y[3]); *(u32x2*)(hn + off + bj * HALF + n * 16) = w; } } }
.LBB0_202:
	s_nop 0
	v_add_u32_e32 v68, 0x80, v116
	v_ashrrev_i32_e32 v69, 31, v68
	v_lshlrev_b64 v[68:69], 12, v[68:69]
	s_waitcnt lgkmcnt(0)
	v_pk_mul_f32 v[62:63], v[62:63], v[66:67] op_sel_hi:[1,0]
	v_pk_mul_f32 v[60:61], v[60:61], v[66:67] op_sel_hi:[1,0]
	v_lshl_add_u64 v[68:69], s[14:15], 0, v[68:69]
	v_pk_mul_f32 v[58:59], v[58:59], v[66:67] op_sel_hi:[1,0]
	v_pk_mul_f32 v[56:57], v[56:57], v[66:67] op_sel_hi:[1,0]
	v_pk_mul_f32 v[54:55], v[54:55], v[66:67] op_sel_hi:[1,0]
	v_pk_mul_f32 v[52:53], v[52:53], v[66:67] op_sel_hi:[1,0]
	v_pk_mul_f32 v[50:51], v[50:51], v[66:67] op_sel_hi:[1,0]
	v_pk_mul_f32 v[48:49], v[48:49], v[66:67] op_sel_hi:[1,0]
	v_pk_mul_f32 v[62:63], v[14:15], v[62:63]
	v_pk_mul_f32 v[60:61], v[12:13], v[60:61]
	v_lshl_add_u64 v[68:69], v[114:115], 2, v[68:69]
	v_pk_mul_f32 v[58:59], v[10:11], v[58:59]
	v_pk_mul_f32 v[56:57], v[8:9], v[56:57]
	v_pk_mul_f32 v[54:55], v[6:7], v[54:55]
	v_pk_mul_f32 v[52:53], v[4:5], v[52:53]
	v_pk_mul_f32 v[50:51], v[2:3], v[50:51]
	v_pk_mul_f32 v[48:49], v[0:1], v[48:49]
	s_and_b64 vcc, exec, s[38:39]
	global_store_dwordx4 v[68:69], v[60:63], off sc1
	global_store_dwordx4 v[68:69], v[56:59], off offset:64 sc1
	global_store_dwordx4 v[68:69], v[52:55], off offset:512 sc1
	global_store_dwordx4 v[68:69], v[48:51], off offset:576 sc1
	s_cbranch_vccnz .LBB0_204
	s_nop 0
	v_lshl_add_u32 v48, v121, 2, 0
	ds_read_b32 v64, v48 offset:4672
.LBB0_204:
	s_nop 0
	v_add_u32_e32 v48, 0x90, v116
	v_ashrrev_i32_e32 v49, 31, v48
	v_lshlrev_b64 v[48:49], 12, v[48:49]
	v_lshl_add_u64 v[48:49], s[14:15], 0, v[48:49]
	s_waitcnt lgkmcnt(0)
	v_pk_mul_f32 v[34:35], v[34:35], v[64:65] op_sel_hi:[1,0]
	v_pk_mul_f32 v[32:33], v[32:33], v[64:65] op_sel_hi:[1,0]
	v_pk_mul_f32 v[46:47], v[46:47], v[64:65] op_sel_hi:[1,0]
	v_pk_mul_f32 v[44:45], v[44:45], v[64:65] op_sel_hi:[1,0]
	v_lshl_add_u64 v[48:49], v[114:115], 2, v[48:49]
	v_pk_mul_f32 v[42:43], v[42:43], v[64:65] op_sel_hi:[1,0]
	v_pk_mul_f32 v[40:41], v[40:41], v[64:65] op_sel_hi:[1,0]
	v_pk_mul_f32 v[38:39], v[38:39], v[64:65] op_sel_hi:[1,0]
	v_pk_mul_f32 v[36:37], v[36:37], v[64:65] op_sel_hi:[1,0]
	v_pk_mul_f32 v[34:35], v[2:3], v[34:35]
	v_pk_mul_f32 v[32:33], v[0:1], v[32:33]
	v_pk_mul_f32 v[46:47], v[14:15], v[46:47]
	v_pk_mul_f32 v[44:45], v[12:13], v[44:45]
	v_pk_mul_f32 v[42:43], v[10:11], v[42:43]
	v_pk_mul_f32 v[40:41], v[8:9], v[40:41]
	v_pk_mul_f32 v[38:39], v[6:7], v[38:39]
	v_pk_mul_f32 v[36:37], v[4:5], v[36:37]
	global_store_dwordx4 v[48:49], v[32:35], off offset:576 sc1
	s_and_b64 vcc, exec, s[38:39]
	global_store_dwordx4 v[48:49], v[44:47], off sc1
	v_mov_b32_e32 v32, 0x7fc00000
	v_mov_b32_e32 v34, 0x7fc00000
	global_store_dwordx4 v[48:49], v[40:43], off offset:64 sc1
	global_store_dwordx4 v[48:49], v[36:39], off offset:512 sc1
	s_cbranch_vccnz .LBB0_206
	v_lshl_add_u32 v33, v121, 2, 0
	ds_read_b32 v34, v33 offset:4736
.LBB0_206:
	s_nop 0
	v_add_u32_e32 v36, 0xa0, v116
	v_ashrrev_i32_e32 v37, 31, v36
	v_lshlrev_b64 v[40:41], 12, v[36:37]
	s_waitcnt lgkmcnt(0)
	v_pk_mul_f32 v[36:37], v[144:145], v[34:35] op_sel_hi:[1,0]
	v_pk_mul_f32 v[42:43], v[142:143], v[34:35] op_sel_hi:[1,0]
	v_lshl_add_u64 v[40:41], s[14:15], 0, v[40:41]
	v_pk_mul_f32 v[38:39], v[14:15], v[36:37]
	v_pk_mul_f32 v[36:37], v[12:13], v[42:43]
	v_lshl_add_u64 v[40:41], v[114:115], 2, v[40:41]
	global_store_dwordx4 v[40:41], v[36:39], off sc1
	v_pk_mul_f32 v[26:27], v[26:27], v[34:35] op_sel_hi:[1,0]
	v_pk_mul_f32 v[22:23], v[22:23], v[34:35] op_sel_hi:[1,0]
	v_pk_mul_f32 v[36:37], v[138:139], v[34:35] op_sel_hi:[1,0]
	v_pk_mul_f32 v[20:21], v[20:21], v[34:35] op_sel_hi:[1,0]
	v_pk_mul_f32 v[18:19], v[18:19], v[34:35] op_sel_hi:[1,0]
	v_pk_mul_f32 v[16:17], v[16:17], v[34:35] op_sel_hi:[1,0]
	v_pk_mul_f32 v[38:39], v[10:11], v[26:27]
	v_pk_mul_f32 v[36:37], v[8:9], v[36:37]
	v_pk_mul_f32 v[22:23], v[6:7], v[22:23]
	v_pk_mul_f32 v[20:21], v[4:5], v[20:21]
	v_pk_mul_f32 v[18:19], v[2:3], v[18:19]
	v_pk_mul_f32 v[16:17], v[0:1], v[16:17]
	s_and_b64 vcc, exec, s[38:39]
	global_store_dwordx4 v[40:41], v[36:39], off offset:64 sc1
	global_store_dwordx4 v[40:41], v[20:23], off offset:512 sc1
	global_store_dwordx4 v[40:41], v[16:19], off offset:576 sc1
	s_cbranch_vccnz .LBB0_208
	s_nop 0
	v_lshl_add_u32 v16, v121, 2, 0
	ds_read_b32 v32, v16 offset:4800
.LBB0_208:
	s_nop 0
	v_add_u32_e32 v16, 0xb0, v116
	v_ashrrev_i32_e32 v17, 31, v16
	v_lshlrev_b64 v[16:17], 12, v[16:17]
	s_waitcnt lgkmcnt(0)
	v_pk_mul_f32 v[18:19], v[128:129], v[32:33] op_sel_hi:[1,0]
	v_pk_mul_f32 v[20:21], v[126:127], v[32:33] op_sel_hi:[1,0]
	v_lshl_add_u64 v[16:17], s[14:15], 0, v[16:17]
	v_pk_mul_f32 v[14:15], v[14:15], v[18:19]
	v_pk_mul_f32 v[12:13], v[12:13], v[20:21]
	v_lshl_add_u64 v[16:17], v[114:115], 2, v[16:17]
	global_store_dwordx4 v[16:17], v[12:15], off sc1
	s_nop 1
	v_pk_mul_f32 v[12:13], v[124:125], v[32:33] op_sel_hi:[1,0]
	v_pk_mul_f32 v[14:15], v[122:123], v[32:33] op_sel_hi:[1,0]
	v_pk_mul_f32 v[10:11], v[10:11], v[12:13]
	v_pk_mul_f32 v[8:9], v[8:9], v[14:15]
	global_store_dwordx4 v[16:17], v[8:11], off offset:64 sc1
	s_nop 1
	v_pk_mul_f32 v[8:9], v[30:31], v[32:33] op_sel_hi:[1,0]
	v_pk_mul_f32 v[10:11], v[118:119], v[32:33] op_sel_hi:[1,0]
	v_pk_mul_f32 v[6:7], v[6:7], v[8:9]
	v_pk_mul_f32 v[4:5], v[4:5], v[10:11]
	global_store_dwordx4 v[16:17], v[4:7], off offset:512 sc1
	s_nop 1
	v_pk_mul_f32 v[4:5], v[24:25], v[32:33] op_sel_hi:[1,0]
	v_pk_mul_f32 v[6:7], v[28:29], v[32:33] op_sel_hi:[1,0]
	v_pk_mul_f32 v[2:3], v[2:3], v[4:5]
	v_pk_mul_f32 v[0:1], v[0:1], v[6:7]
	global_store_dwordx4 v[16:17], v[0:3], off offset:576 sc1

; __device__ __forceinline__ unsigned cvt_pk_f16(float lo, float hi) { f32x2 v = {lo, hi}; h16x2 b = __builtin_convertvector(v, h16x2); return __builtin_bit_cast(unsigned, b); }
;     __device__ __forceinline__ void fused(f32x4 (&acc)[2][2][4][2], const Unit& u, int wr, int wc, int fr, int fq, PG8_LAS unsigned char* lds, int wid, int lane) const {
;     ...
;             for (int m = 0; m < 4; ++m) { const int r = ai * HALF + wr * 64 + m * 16 + fr2; const float rstd = bad ? qnan : S[r]; const size_t off = (size_t)(u.pm * BM + r) * DM + col2;
; #pragma unroll
;                 for (int bj = 0; bj < 2; ++bj)
; #pragma unroll
;                     for (int n = 0; n < 2; ++n) { const f32x4 x1 = acc[ai][bj][m][n]; const f32x4 y = x1 * rstd * gv[bj][n];
;                         if (FINAL) *(f32x4*)(out + off + bj * HALF + n * 16) = y;
;                         else { *(f32x4*)(out + off + bj * HALF + n * 16) = x1;
;                             typedef unsigned u32x2 __attribute__((ext_vector_type(2)));
;                             u32x2 w; w.x = cvt_pk_f16(y[0], y[1]); w.y = cvt_pk_f16(y[2], y[3]); *(u32x2*)(hn + off + bj * HALF + n * 16) = w; } } }
.LBB0_273:
	v_readlane_b32 s36, v252, 3
	v_readlane_b32 s42, v252, 9
	v_readlane_b32 s43, v252, 10
	s_add_u32 s2, s42, s14
	s_addc_u32 s3, s43, s15
	v_readlane_b32 s5, v255, 42
	v_add_u32_e32 v148, s10, v151
	s_cmp_eq_u32 s5, 0
	s_mov_b32 s5, 0x3400000
	v_ashrrev_i32_e32 v149, 31, v148
	s_cselect_b32 s5, s5, 0x1a400000
	v_readlane_b32 s12, v252, 1
	v_lshlrev_b64 v[152:153], 10, v[148:149]
	v_readlane_b32 s13, v252, 2
	s_add_u32 s14, s12, s5
	v_lshl_add_u64 v[152:153], v[152:153], 0, v[146:147]
	s_waitcnt lgkmcnt(0)
	v_pk_mul_f32 v[154:155], v[128:129], v[150:151] op_sel_hi:[1,0]
	v_pk_mul_f32 v[156:157], v[126:127], v[150:151] op_sel_hi:[1,0]
	s_addc_u32 s15, s13, 0
	s_waitcnt vmcnt(3)
	v_pk_mul_f32 v[154:155], v[144:145], v[154:155]
	v_pk_mul_f32 v[156:157], v[142:143], v[156:157]
	v_lshl_add_u64 v[158:159], v[152:153], 2, s[2:3]
	global_store_dwordx4 v[158:159], v[126:129], off sc1
	v_readlane_b32 s38, v252, 5
	v_readlane_b32 s39, v252, 6
	v_cvt_pk_f16_f32 v126, v156, v157
	v_cvt_pk_f16_f32 v127, v154, v155
	v_lshl_add_u64 v[128:129], v[152:153], 1, s[14:15]
	global_store_dwordx2 v[128:129], v[126:127], off sc1
	v_pk_mul_f32 v[126:127], v[124:125], v[150:151] op_sel_hi:[1,0]
	v_pk_mul_f32 v[152:153], v[122:123], v[150:151] op_sel_hi:[1,0]
	s_waitcnt vmcnt(4)
	v_pk_mul_f32 v[126:127], v[140:141], v[126:127]
	v_pk_mul_f32 v[152:153], v[138:139], v[152:153]
	global_store_dwordx4 v[158:159], v[122:125], off offset:64 sc1
	s_andn2_b64 vcc, exec, s[0:1]
	v_readlane_b32 s37, v252, 4
	v_cvt_pk_f16_f32 v122, v152, v153
	v_cvt_pk_f16_f32 v123, v126, v127
	global_store_dwordx2 v[128:129], v[122:123], off offset:32 sc1
	v_pk_mul_f32 v[122:123], v[120:121], v[150:151] op_sel_hi:[1,0]
	v_pk_mul_f32 v[124:125], v[118:119], v[150:151] op_sel_hi:[1,0]
	s_waitcnt vmcnt(5)
	v_pk_mul_f32 v[122:123], v[136:137], v[122:123]
	v_pk_mul_f32 v[124:125], v[134:135], v[124:125]
	global_store_dwordx4 v[158:159], v[118:121], off offset:512 sc1
	v_readlane_b32 s40, v252, 7
	v_readlane_b32 s41, v252, 8
	v_cvt_pk_f16_f32 v118, v124, v125
	v_cvt_pk_f16_f32 v119, v122, v123
	global_store_dwordx2 v[128:129], v[118:119], off offset:256 sc1
	v_pk_mul_f32 v[118:119], v[116:117], v[150:151] op_sel_hi:[1,0]
	v_pk_mul_f32 v[120:121], v[114:115], v[150:151] op_sel_hi:[1,0]
	s_waitcnt vmcnt(6)
	v_pk_mul_f32 v[118:119], v[132:133], v[118:119]
	v_pk_mul_f32 v[120:121], v[130:131], v[120:121]
	global_store_dwordx4 v[158:159], v[114:117], off offset:576 sc1
	s_nop 1
	v_cndmask_b32_e64 v116, 0, 1, s[0:1]
	v_cvt_pk_f16_f32 v114, v120, v121
	v_cvt_pk_f16_f32 v115, v118, v119
	v_cmp_ne_u32_e64 s[38:39], 1, v116
	global_store_dwordx2 v[128:129], v[114:115], off offset:288 sc1
	s_cbranch_vccnz .LBB0_275
	v_lshl_add_u32 v96, v151, 2, 0
	ds_read_b32 v96, v96 offset:4160
.LBB0_275:
	v_add3_u32 v114, s10, v151, 16
	v_ashrrev_i32_e32 v115, 31, v114
	v_lshlrev_b64 v[114:115], 10, v[114:115]
	v_lshl_add_u64 v[114:115], v[114:115], 0, v[146:147]
	s_waitcnt lgkmcnt(0)
	v_pk_mul_f32 v[116:117], v[112:113], v[96:97] op_sel_hi:[1,0]
	v_pk_mul_f32 v[118:119], v[110:111], v[96:97] op_sel_hi:[1,0]
	v_pk_mul_f32 v[116:117], v[144:145], v[116:117]
	v_pk_mul_f32 v[118:119], v[142:143], v[118:119]
	v_lshl_add_u64 v[120:121], v[114:115], 2, s[2:3]
	global_store_dwordx4 v[120:121], v[110:113], off sc1
	s_and_b64 vcc, exec, s[38:39]
	s_nop 0
	v_cvt_pk_f16_f32 v110, v118, v119
	v_cvt_pk_f16_f32 v111, v116, v117
	v_lshl_add_u64 v[112:113], v[114:115], 1, s[14:15]
	global_store_dwordx2 v[112:113], v[110:111], off sc1
	v_pk_mul_f32 v[110:111], v[108:109], v[96:97] op_sel_hi:[1,0]
	v_pk_mul_f32 v[114:115], v[106:107], v[96:97] op_sel_hi:[1,0]
	v_pk_mul_f32 v[110:111], v[140:141], v[110:111]
	v_pk_mul_f32 v[114:115], v[138:139], v[114:115]
	global_store_dwordx4 v[120:121], v[106:109], off offset:64 sc1
	s_nop 1
	v_cvt_pk_f16_f32 v106, v114, v115
	v_cvt_pk_f16_f32 v107, v110, v111
	global_store_dwordx2 v[112:113], v[106:107], off offset:32 sc1
	v_pk_mul_f32 v[106:107], v[104:105], v[96:97] op_sel_hi:[1,0]
	v_pk_mul_f32 v[108:109], v[102:103], v[96:97] op_sel_hi:[1,0]
	v_pk_mul_f32 v[106:107], v[136:137], v[106:107]
	v_pk_mul_f32 v[108:109], v[134:135], v[108:109]
	global_store_dwordx4 v[120:121], v[102:105], off offset:512 sc1
	s_nop 1
	v_cvt_pk_f16_f32 v102, v108, v109
	v_cvt_pk_f16_f32 v103, v106, v107
	global_store_dwordx2 v[112:113], v[102:103], off offset:256 sc1
	v_pk_mul_f32 v[102:103], v[100:101], v[96:97] op_sel_hi:[1,0]
	v_pk_mul_f32 v[104:105], v[98:99], v[96:97] op_sel_hi:[1,0]
	v_pk_mul_f32 v[102:103], v[132:133], v[102:103]
	v_pk_mul_f32 v[104:105], v[130:131], v[104:105]
	global_store_dwordx4 v[120:121], v[98:101], off offset:576 sc1
	v_mov_b32_e32 v96, 0x7fc00000
	s_nop 0
	v_cvt_pk_f16_f32 v98, v104, v105
	v_cvt_pk_f16_f32 v99, v102, v103
	global_store_dwordx2 v[112:113], v[98:99], off offset:288 sc1
	v_mov_b32_e32 v98, 0x7fc00000
	s_cbranch_vccnz .LBB0_277
	v_lshl_add_u32 v98, v151, 2, 0
	ds_read_b32 v98, v98 offset:4224
; __device__ __forceinline__ unsigned cvt_pk_f16(float lo, float hi) { f32x2 v = {lo, hi}; h16x2 b = __builtin_convertvector(v, h16x2); return __builtin_bit_cast(unsigned, b); }
;     __device__ __forceinline__ void fused(f32x4 (&acc)[2][2][4][2], const Unit& u, int wr, int wc, int fr, int fq, PG8_LAS unsigned char* lds, int wid, int lane) const {
;     ...
;             for (int m = 0; m < 4; ++m) { const int r = ai * HALF + wr * 64 + m * 16 + fr2; const float rstd = bad ? qnan : S[r]; const size_t off = (size_t)(u.pm * BM + r) * DM + col2;
; #pragma unroll
;                 for (int bj = 0; bj < 2; ++bj)
; #pragma unroll
;                     for (int n = 0; n < 2; ++n) { const f32x4 x1 = acc[ai][bj][m][n]; const f32x4 y = x1 * rstd * gv[bj][n];
;                         if (FINAL) *(f32x4*)(out + off + bj * HALF + n * 16) = y;
;                         else { *(f32x4*)(out + off + bj * HALF + n * 16) = x1;
;                             typedef unsigned u32x2 __attribute__((ext_vector_type(2)));
;                             u32x2 w; w.x = cvt_pk_f16(y[0], y[1]); w.y = cvt_pk_f16(y[2], y[3]); *(u32x2*)(hn + off + bj * HALF + n * 16) = w; } } }
.LBB0_277:
	v_add3_u32 v100, s10, v151, 32
	v_ashrrev_i32_e32 v101, 31, v100
	v_lshlrev_b64 v[100:101], 10, v[100:101]
	v_lshl_add_u64 v[100:101], v[100:101], 0, v[146:147]
	s_waitcnt lgkmcnt(0)
	v_pk_mul_f32 v[102:103], v[94:95], v[98:99] op_sel_hi:[1,0]
	v_pk_mul_f32 v[104:105], v[92:93], v[98:99] op_sel_hi:[1,0]
	v_pk_mul_f32 v[102:103], v[144:145], v[102:103]
	v_pk_mul_f32 v[104:105], v[142:143], v[104:105]
	v_lshl_add_u64 v[106:107], v[100:101], 2, s[2:3]
	global_store_dwordx4 v[106:107], v[92:95], off sc1
	s_and_b64 vcc, exec, s[38:39]
	s_nop 0
	v_cvt_pk_f16_f32 v92, v104, v105
	v_cvt_pk_f16_f32 v93, v102, v103
	v_lshl_add_u64 v[94:95], v[100:101], 1, s[14:15]
	global_store_dwordx2 v[94:95], v[92:93], off sc1
	v_pk_mul_f32 v[92:93], v[90:91], v[98:99] op_sel_hi:[1,0]
	v_pk_mul_f32 v[100:101], v[88:89], v[98:99] op_sel_hi:[1,0]
	v_pk_mul_f32 v[92:93], v[140:141], v[92:93]
	v_pk_mul_f32 v[100:101], v[138:139], v[100:101]
	global_store_dwordx4 v[106:107], v[88:91], off offset:64 sc1
	s_nop 1
	v_cvt_pk_f16_f32 v88, v100, v101
	v_cvt_pk_f16_f32 v89, v92, v93
	global_store_dwordx2 v[94:95], v[88:89], off offset:32 sc1
	v_pk_mul_f32 v[88:89], v[86:87], v[98:99] op_sel_hi:[1,0]
	v_pk_mul_f32 v[90:91], v[84:85], v[98:99] op_sel_hi:[1,0]
	v_pk_mul_f32 v[88:89], v[136:137], v[88:89]
	v_pk_mul_f32 v[90:91], v[134:135], v[90:91]
	global_store_dwordx4 v[106:107], v[84:87], off offset:512 sc1
	s_nop 1
	v_cvt_pk_f16_f32 v84, v90, v91
	v_cvt_pk_f16_f32 v85, v88, v89
	global_store_dwordx2 v[94:95], v[84:85], off offset:256 sc1
	v_pk_mul_f32 v[84:85], v[82:83], v[98:99] op_sel_hi:[1,0]
	v_pk_mul_f32 v[86:87], v[80:81], v[98:99] op_sel_hi:[1,0]
	v_pk_mul_f32 v[84:85], v[132:133], v[84:85]
	v_pk_mul_f32 v[86:87], v[130:131], v[86:87]
	global_store_dwordx4 v[106:107], v[80:83], off offset:576 sc1
	s_nop 1
	v_cvt_pk_f16_f32 v80, v86, v87
	v_cvt_pk_f16_f32 v81, v84, v85
	global_store_dwordx2 v[94:95], v[80:81], off offset:288 sc1
	s_cbranch_vccnz .LBB0_279
	v_lshl_add_u32 v80, v151, 2, 0
	ds_read_b32 v96, v80 offset:4288
.LBB0_279:
	v_add3_u32 v80, s10, v151, 48
	v_ashrrev_i32_e32 v81, 31, v80
	v_lshlrev_b64 v[80:81], 10, v[80:81]
	v_lshl_add_u64 v[80:81], v[80:81], 0, v[146:147]
	s_waitcnt lgkmcnt(0)
	v_pk_mul_f32 v[82:83], v[78:79], v[96:97] op_sel_hi:[1,0]
	v_pk_mul_f32 v[84:85], v[76:77], v[96:97] op_sel_hi:[1,0]
	v_pk_mul_f32 v[82:83], v[144:145], v[82:83]
	v_pk_mul_f32 v[84:85], v[142:143], v[84:85]
	v_lshl_add_u64 v[86:87], v[80:81], 2, s[2:3]
	global_store_dwordx4 v[86:87], v[76:79], off sc1
	s_and_b64 vcc, exec, s[38:39]
	s_nop 0
	v_cvt_pk_f16_f32 v76, v84, v85
	v_cvt_pk_f16_f32 v77, v82, v83
	v_lshl_add_u64 v[78:79], v[80:81], 1, s[14:15]
	global_store_dwordx2 v[78:79], v[76:77], off sc1
	v_pk_mul_f32 v[76:77], v[74:75], v[96:97] op_sel_hi:[1,0]
	v_pk_mul_f32 v[80:81], v[72:73], v[96:97] op_sel_hi:[1,0]
	v_pk_mul_f32 v[76:77], v[140:141], v[76:77]
	v_pk_mul_f32 v[80:81], v[138:139], v[80:81]
	global_store_dwordx4 v[86:87], v[72:75], off offset:64 sc1
	s_nop 1
	v_cvt_pk_f16_f32 v72, v80, v81
	v_cvt_pk_f16_f32 v73, v76, v77
	global_store_dwordx2 v[78:79], v[72:73], off offset:32 sc1
	v_pk_mul_f32 v[72:73], v[70:71], v[96:97] op_sel_hi:[1,0]
	v_pk_mul_f32 v[74:75], v[68:69], v[96:97] op_sel_hi:[1,0]
	v_pk_mul_f32 v[72:73], v[136:137], v[72:73]
	v_pk_mul_f32 v[74:75], v[134:135], v[74:75]
	global_store_dwordx4 v[86:87], v[68:71], off offset:512 sc1
	s_nop 1
	v_cvt_pk_f16_f32 v68, v74, v75
	v_cvt_pk_f16_f32 v69, v72, v73
	global_store_dwordx2 v[78:79], v[68:69], off offset:256 sc1
	v_pk_mul_f32 v[68:69], v[66:67], v[96:97] op_sel_hi:[1,0]
	v_pk_mul_f32 v[70:71], v[64:65], v[96:97] op_sel_hi:[1,0]
	v_pk_mul_f32 v[68:69], v[132:133], v[68:69]
	v_pk_mul_f32 v[70:71], v[130:131], v[70:71]
	global_store_dwordx4 v[86:87], v[64:67], off offset:576 sc1
	s_nop 1
	v_cvt_pk_f16_f32 v64, v70, v71
	v_cvt_pk_f16_f32 v65, v68, v69
	global_store_dwordx2 v[78:79], v[64:65], off offset:288 sc1
	v_mov_b32_e32 v64, 0x7fc00000
	v_mov_b32_e32 v66, 0x7fc00000
	s_cbranch_vccnz .LBB0_281
	v_lshl_add_u32 v65, v151, 2, 0
	ds_read_b32 v66, v65 offset:4608
.LBB0_281:
	v_add_u32_e32 v68, 0x80, v148
	v_ashrrev_i32_e32 v69, 31, v68
	v_lshlrev_b64 v[68:69], 10, v[68:69]
	v_lshl_add_u64 v[68:69], v[68:69], 0, v[146:147]
	s_waitcnt lgkmcnt(0)
	v_pk_mul_f32 v[70:71], v[62:63], v[66:67] op_sel_hi:[1,0]
	v_pk_mul_f32 v[72:73], v[60:61], v[66:67] op_sel_hi:[1,0]
	v_pk_mul_f32 v[70:71], v[144:145], v[70:71]
	v_pk_mul_f32 v[72:73], v[142:143], v[72:73]
	v_lshl_add_u64 v[74:75], v[68:69], 2, s[2:3]
	global_store_dwordx4 v[74:75], v[60:63], off sc1
	s_and_b64 vcc, exec, s[38:39]
	s_nop 0
	v_cvt_pk_f16_f32 v60, v72, v73
	v_cvt_pk_f16_f32 v61, v70, v71
	v_lshl_add_u64 v[62:63], v[68:69], 1, s[14:15]
	global_store_dwordx2 v[62:63], v[60:61], off sc1
	v_pk_mul_f32 v[60:61], v[58:59], v[66:67] op_sel_hi:[1,0]
	v_pk_mul_f32 v[68:69], v[56:57], v[66:67] op_sel_hi:[1,0]
	v_pk_mul_f32 v[60:61], v[140:141], v[60:61]
	v_pk_mul_f32 v[68:69], v[138:139], v[68:69]
	global_store_dwordx4 v[74:75], v[56:59], off offset:64 sc1
	s_nop 1
	v_cvt_pk_f16_f32 v56, v68, v69
	v_cvt_pk_f16_f32 v57, v60, v61
	global_store_dwordx2 v[62:63], v[56:57], off offset:32 sc1
	v_pk_mul_f32 v[56:57], v[54:55], v[66:67] op_sel_hi:[1,0]
	v_pk_mul_f32 v[58:59], v[52:53], v[66:67] op_sel_hi:[1,0]
	v_pk_mul_f32 v[56:57], v[136:137], v[56:57]
	v_pk_mul_f32 v[58:59], v[134:135], v[58:59]
	global_store_dwordx4 v[74:75], v[52:55], off offset:512 sc1
	s_nop 1
	v_cvt_pk_f16_f32 v52, v58, v59
	v_cvt_pk_f16_f32 v53, v56, v57
	global_store_dwordx2 v[62:63], v[52:53], off offset:256 sc1
	v_pk_mul_f32 v[52:53], v[50:51], v[66:67] op_sel_hi:[1,0]
	v_pk_mul_f32 v[54:55], v[48:49], v[66:67] op_sel_hi:[1,0]
	v_pk_mul_f32 v[52:53], v[132:133], v[52:53]
	v_pk_mul_f32 v[54:55], v[130:131], v[54:55]
	global_store_dwordx4 v[74:75], v[48:51], off offset:576 sc1
	s_nop 1
	v_cvt_pk_f16_f32 v48, v54, v55
	v_cvt_pk_f16_f32 v49, v52, v53
	global_store_dwordx2 v[62:63], v[48:49], off offset:288 sc1
	s_cbranch_vccnz .LBB0_283
	v_lshl_add_u32 v48, v151, 2, 0
	ds_read_b32 v64, v48 offset:4672
; __device__ __forceinline__ unsigned cvt_pk_f16(float lo, float hi) { f32x2 v = {lo, hi}; h16x2 b = __builtin_convertvector(v, h16x2); return __builtin_bit_cast(unsigned, b); }
;     __device__ __forceinline__ void fused(f32x4 (&acc)[2][2][4][2], const Unit& u, int wr, int wc, int fr, int fq, PG8_LAS unsigned char* lds, int wid, int lane) const {
;     ...
;             for (int m = 0; m < 4; ++m) { const int r = ai * HALF + wr * 64 + m * 16 + fr2; const float rstd = bad ? qnan : S[r]; const size_t off = (size_t)(u.pm * BM + r) * DM + col2;
; #pragma unroll
;                 for (int bj = 0; bj < 2; ++bj)
; #pragma unroll
;                     for (int n = 0; n < 2; ++n) { const f32x4 x1 = acc[ai][bj][m][n]; const f32x4 y = x1 * rstd * gv[bj][n];
;                         if (FINAL) *(f32x4*)(out + off + bj * HALF + n * 16) = y;
;                         else { *(f32x4*)(out + off + bj * HALF + n * 16) = x1;
;                             typedef unsigned u32x2 __attribute__((ext_vector_type(2)));
;                             u32x2 w; w.x = cvt_pk_f16(y[0], y[1]); w.y = cvt_pk_f16(y[2], y[3]); *(u32x2*)(hn + off + bj * HALF + n * 16) = w; } } }
.LBB0_283:
	v_add_u32_e32 v48, 0x90, v148
	v_ashrrev_i32_e32 v49, 31, v48
	v_lshlrev_b64 v[48:49], 10, v[48:49]
	v_lshl_add_u64 v[48:49], v[48:49], 0, v[146:147]
	s_waitcnt lgkmcnt(0)
	v_pk_mul_f32 v[50:51], v[46:47], v[64:65] op_sel_hi:[1,0]
	v_pk_mul_f32 v[52:53], v[44:45], v[64:65] op_sel_hi:[1,0]
	v_pk_mul_f32 v[50:51], v[144:145], v[50:51]
	v_pk_mul_f32 v[52:53], v[142:143], v[52:53]
	v_lshl_add_u64 v[54:55], v[48:49], 2, s[2:3]
	global_store_dwordx4 v[54:55], v[44:47], off sc1
	s_and_b64 vcc, exec, s[38:39]
	s_nop 0
	v_cvt_pk_f16_f32 v44, v52, v53
	v_cvt_pk_f16_f32 v45, v50, v51
	v_lshl_add_u64 v[46:47], v[48:49], 1, s[14:15]
	global_store_dwordx2 v[46:47], v[44:45], off sc1
	v_pk_mul_f32 v[44:45], v[42:43], v[64:65] op_sel_hi:[1,0]
	v_pk_mul_f32 v[48:49], v[40:41], v[64:65] op_sel_hi:[1,0]
	v_pk_mul_f32 v[44:45], v[140:141], v[44:45]
	v_pk_mul_f32 v[48:49], v[138:139], v[48:49]
	global_store_dwordx4 v[54:55], v[40:43], off offset:64 sc1
	s_nop 1
	v_cvt_pk_f16_f32 v40, v48, v49
	v_cvt_pk_f16_f32 v41, v44, v45
	global_store_dwordx2 v[46:47], v[40:41], off offset:32 sc1
	v_pk_mul_f32 v[40:41], v[38:39], v[64:65] op_sel_hi:[1,0]
	v_pk_mul_f32 v[42:43], v[36:37], v[64:65] op_sel_hi:[1,0]
	v_pk_mul_f32 v[40:41], v[136:137], v[40:41]
	v_pk_mul_f32 v[42:43], v[134:135], v[42:43]
	global_store_dwordx4 v[54:55], v[36:39], off offset:512 sc1
	s_nop 1
	v_cvt_pk_f16_f32 v36, v42, v43
	v_cvt_pk_f16_f32 v37, v40, v41
	global_store_dwordx2 v[46:47], v[36:37], off offset:256 sc1
	v_pk_mul_f32 v[36:37], v[34:35], v[64:65] op_sel_hi:[1,0]
	v_pk_mul_f32 v[38:39], v[32:33], v[64:65] op_sel_hi:[1,0]
	v_pk_mul_f32 v[36:37], v[132:133], v[36:37]
	v_pk_mul_f32 v[38:39], v[130:131], v[38:39]
	global_store_dwordx4 v[54:55], v[32:35], off offset:576 sc1
	s_nop 1
	v_cvt_pk_f16_f32 v32, v38, v39
	v_cvt_pk_f16_f32 v33, v36, v37
	global_store_dwordx2 v[46:47], v[32:33], off offset:288 sc1
	v_mov_b32_e32 v32, 0x7fc00000
	v_mov_b32_e32 v34, 0x7fc00000
	s_cbranch_vccnz .LBB0_285
	v_lshl_add_u32 v33, v151, 2, 0
	ds_read_b32 v34, v33 offset:4736
.LBB0_285:
	v_add_u32_e32 v36, 0xa0, v148
	v_ashrrev_i32_e32 v37, 31, v36
	v_lshlrev_b64 v[36:37], 10, v[36:37]
	v_lshl_add_u64 v[36:37], v[36:37], 0, v[146:147]
	s_waitcnt lgkmcnt(0)
	v_pk_mul_f32 v[38:39], v[30:31], v[34:35] op_sel_hi:[1,0]
	v_pk_mul_f32 v[40:41], v[28:29], v[34:35] op_sel_hi:[1,0]
	v_pk_mul_f32 v[38:39], v[144:145], v[38:39]
	v_pk_mul_f32 v[40:41], v[142:143], v[40:41]
	v_lshl_add_u64 v[42:43], v[36:37], 2, s[2:3]
	global_store_dwordx4 v[42:43], v[28:31], off sc1
	s_and_b64 vcc, exec, s[38:39]
	s_nop 0
	v_cvt_pk_f16_f32 v28, v40, v41
	v_cvt_pk_f16_f32 v29, v38, v39
	v_lshl_add_u64 v[30:31], v[36:37], 1, s[14:15]
	global_store_dwordx2 v[30:31], v[28:29], off sc1
	v_pk_mul_f32 v[28:29], v[26:27], v[34:35] op_sel_hi:[1,0]
	v_pk_mul_f32 v[36:37], v[24:25], v[34:35] op_sel_hi:[1,0]
	v_pk_mul_f32 v[28:29], v[140:141], v[28:29]
	v_pk_mul_f32 v[36:37], v[138:139], v[36:37]
	global_store_dwordx4 v[42:43], v[24:27], off offset:64 sc1
	s_nop 1
	v_cvt_pk_f16_f32 v24, v36, v37
	v_cvt_pk_f16_f32 v25, v28, v29
	global_store_dwordx2 v[30:31], v[24:25], off offset:32 sc1
	v_pk_mul_f32 v[24:25], v[22:23], v[34:35] op_sel_hi:[1,0]
	v_pk_mul_f32 v[26:27], v[20:21], v[34:35] op_sel_hi:[1,0]
	v_pk_mul_f32 v[24:25], v[136:137], v[24:25]
	v_pk_mul_f32 v[26:27], v[134:135], v[26:27]
	global_store_dwordx4 v[42:43], v[20:23], off offset:512 sc1
	s_nop 1
	v_cvt_pk_f16_f32 v20, v26, v27
	v_cvt_pk_f16_f32 v21, v24, v25
	global_store_dwordx2 v[30:31], v[20:21], off offset:256 sc1
	v_pk_mul_f32 v[20:21], v[18:19], v[34:35] op_sel_hi:[1,0]
	v_pk_mul_f32 v[22:23], v[16:17], v[34:35] op_sel_hi:[1,0]
	v_pk_mul_f32 v[20:21], v[132:133], v[20:21]
	v_pk_mul_f32 v[22:23], v[130:131], v[22:23]
	global_store_dwordx4 v[42:43], v[16:19], off offset:576 sc1
	s_nop 1
	v_cvt_pk_f16_f32 v16, v22, v23
	v_cvt_pk_f16_f32 v17, v20, v21
	global_store_dwordx2 v[30:31], v[16:17], off offset:288 sc1
	s_cbranch_vccnz .LBB0_287
	v_lshl_add_u32 v16, v151, 2, 0
	ds_read_b32 v32, v16 offset:4800
.LBB0_287:
	v_add_u32_e32 v16, 0xb0, v148
	v_ashrrev_i32_e32 v17, 31, v16
	v_lshlrev_b64 v[16:17], 10, v[16:17]
	v_lshl_add_u64 v[16:17], v[16:17], 0, v[146:147]
	s_waitcnt lgkmcnt(0)
	v_pk_mul_f32 v[18:19], v[14:15], v[32:33] op_sel_hi:[1,0]
	v_pk_mul_f32 v[20:21], v[12:13], v[32:33] op_sel_hi:[1,0]
	v_pk_mul_f32 v[18:19], v[144:145], v[18:19]
	v_pk_mul_f32 v[20:21], v[142:143], v[20:21]
	v_lshl_add_u64 v[22:23], v[16:17], 2, s[2:3]
	global_store_dwordx4 v[22:23], v[12:15], off sc1
	s_nop 1
	v_cvt_pk_f16_f32 v12, v20, v21
	v_cvt_pk_f16_f32 v13, v18, v19
	v_lshl_add_u64 v[14:15], v[16:17], 1, s[14:15]
	global_store_dwordx2 v[14:15], v[12:13], off sc1
	v_pk_mul_f32 v[12:13], v[10:11], v[32:33] op_sel_hi:[1,0]
	v_pk_mul_f32 v[16:17], v[8:9], v[32:33] op_sel_hi:[1,0]
	v_pk_mul_f32 v[12:13], v[140:141], v[12:13]
	v_pk_mul_f32 v[16:17], v[138:139], v[16:17]
	global_store_dwordx4 v[22:23], v[8:11], off offset:64 sc1
	s_nop 1
	v_cvt_pk_f16_f32 v8, v16, v17
	v_cvt_pk_f16_f32 v9, v12, v13
	global_store_dwordx2 v[14:15], v[8:9], off offset:32 sc1
	v_pk_mul_f32 v[8:9], v[6:7], v[32:33] op_sel_hi:[1,0]
	v_pk_mul_f32 v[10:11], v[4:5], v[32:33] op_sel_hi:[1,0]
	v_pk_mul_f32 v[8:9], v[136:137], v[8:9]
	v_pk_mul_f32 v[10:11], v[134:135], v[10:11]
	global_store_dwordx4 v[22:23], v[4:7], off offset:512 sc1
	s_nop 1
	v_cvt_pk_f16_f32 v4, v10, v11
	v_cvt_pk_f16_f32 v5, v8, v9
	global_store_dwordx2 v[14:15], v[4:5], off offset:256 sc1
	v_pk_mul_f32 v[4:5], v[2:3], v[32:33] op_sel_hi:[1,0]
	v_pk_mul_f32 v[6:7], v[0:1], v[32:33] op_sel_hi:[1,0]
	v_pk_mul_f32 v[4:5], v[132:133], v[4:5]
	v_pk_mul_f32 v[6:7], v[130:131], v[6:7]
	global_store_dwordx4 v[22:23], v[0:3], off offset:576 sc1
	s_nop 1
	v_cvt_pk_f16_f32 v0, v6, v7
	v_cvt_pk_f16_f32 v1, v4, v5
	global_store_dwordx2 v[14:15], v[0:1], off offset:288 sc1
